# GEMM1 unit boundaries: weight side-stream consume scales with packed multiplies (16 instead of 32 + 8 dead moves)
# baseline (speedup 1.0000x reference)
.LBB0_896:
	v_readlane_b32 s3, v254, 10
	s_lshl_b32 s59, s2, 6
	v_ashrrev_i32_e32 v4, 5, v2
	s_lshl_b32 s2, s2, 13
	v_lshlrev_b32_e32 v1, 1, v2
	v_lshl_add_u32 v5, v4, 10, s2
	s_lshl_b32 s2, s3, 5
	v_and_b32_e32 v3, 32, v1
	v_lshlrev_b32_e32 v2, 6, v2
	s_and_b32 s60, s2, 0x60
	v_or_b32_e32 v6, v5, v3
	v_and_b32_e32 v2, 0x3c0, v2
	v_and_b32_e32 v1, 16, v1
	s_lshr_b32 s2, s60, 3
	v_or3_b32 v6, v6, v2, v1
	v_add_lshl_u32 v4, v4, s2, 10
	v_or_b32_e32 v2, v2, v3
	v_or3_b32 v194, v2, v4, v1
	v_or_b32_e32 v2, 16, v2
	v_mov_b32_e32 v177, 0
	v_bitop3_b32 v5, v2, v5, v1 bitop3:0xde
	v_bitop3_b32 v195, v2, v4, v1 bitop3:0xde
	v_mbcnt_lo_u32_b32 v1, -1, 0
	v_mbcnt_hi_u32_b32 v1, -1, v1
	v_and_b32_e32 v4, 15, v1
	v_lshrrev_b32_e32 v1, 4, v1
	v_lshlrev_b32_e32 v1, 1, v1
	v_bfe_u32 v194, v4, 1, 3
	v_and_b32_e32 v194, 5, v194
	v_xor_b32_e32 v1, v1, v194
	v_lshlrev_b32_e32 v1, 4, v1
	v_lshl_add_u32 v1, v4, 7, v1
	v_lshl_add_u32 v6, s59, 7, v1
	v_xor_b32_e32 v5, 16, v6
	v_lshl_add_u32 v194, s60, 7, v1
	v_xor_b32_e32 v195, 16, v194
	s_waitcnt vmcnt(2)
	s_barrier
	s_mov_b64 s[14:15], 0x80
	v_lshl_add_u64 v[2:3], s[36:37], 0, v[176:177]
	s_add_i32 m0, s50, 0x18000
	v_lshl_add_u64 v[2:3], v[2:3], 0, s[14:15]
	s_add_i32 s58, s3, s49
	global_load_lds_dwordx4 v[2:3], off
	v_mov_b32_e32 v179, v177
	s_add_i32 m0, s50, 0x1a000
	s_add_u32 s2, s10, 0x36000080
	v_lshl_add_u64 v[2:3], s[36:37], 0, v[178:179]
	v_lshl_add_u64 v[2:3], v[2:3], 0, s[14:15]
	s_addc_u32 s3, s11, 0
	s_add_i32 s62, s50, 0x8000
	global_load_lds_dwordx4 v[2:3], off
	s_mov_b32 m0, s62
	s_add_i32 s63, s50, 0xa000
	s_mov_b64 s[16:17], 0x36000080
	global_load_lds_dwordx4 v180, s[2:3]
	s_mov_b32 m0, s63
	s_mov_b32 s61, 0x8000
	global_load_lds_dwordx4 v182, s[2:3]
	s_add_u32 s2, s36, 0x4080
	s_addc_u32 s3, s37, 0
	s_add_i32 m0, s50, 0x1c000
	s_movk_i32 s64, 0x100
	global_load_lds_dwordx4 v176, s[2:3]
	s_add_i32 m0, s50, 0x1e000
	v_mov_b32_e32 v184, v176
	global_load_lds_dwordx4 v178, s[2:3]
	s_waitcnt vmcnt(6)
	v_readlane_b32 s2, v254, 15
	s_cmpk_lt_u32 s2, 0x100
	s_cselect_b64 s[18:19], -1, 0
	s_add_i32 s65, s45, -1
	v_mov_b32_e32 v231, 0x24854
	v_mov_b32_e32 v252, 0x24858
	v_mov_b32_e32 v253, 0x2485c
	v_mov_b32_e32 v220, 0x24864
	v_mov_b32_e32 v221, 0x24868
	v_mov_b32_e32 v222, 0x2486c
	v_mov_b32_e32 v223, 0x24870
	v_mov_b32_e32 v224, 0x24874
	v_mov_b32_e32 v225, 0x24878
	v_mov_b32_e32 v226, 0x2487c
	s_mov_b32 s66, 0x25800
	s_add_i32 s67, 0, 0x10000
	s_add_i32 s68, 0, 0x14000
	v_add_u32_e32 v227, 0, v6
	v_add_u32_e32 v228, 0, v5
	v_mov_b32_e32 v229, 0x7f7f7f7f
	v_add_u32_e32 v220, 0x10000, v194
	v_add_u32_e32 v221, 0x10000, v195
	v_add_u32_e32 v222, 0x14000, v194
	v_add_u32_e32 v223, 0x14000, v195
	v_add_u32_e32 v224, 0x18000, v194
	v_add_u32_e32 v225, 0x18000, v195
	v_add_u32_e32 v226, 0x1c000, v194
	v_add_u32_e32 v229, 0x1c000, v195
	v_mov_b32_e32 v252, 0x43800000
	v_mov_b32_e32 v253, 0x43800000
	s_mov_b64 s[20:21], 0x5e000000
	s_mov_b32 s69, 0xc0c00000
	s_mov_b64 s[22:23], 0x22000000
	s_mov_b32 s70, 0x22001000
	v_mov_b32_e32 v230, 0x41000000
	v_mov_b32_e32 v176, v0
	s_mov_b32 s74, 0
	v_mov_b32_e32 v0, v177
	v_mov_b32_e32 v1, v177
	v_mov_b32_e32 v2, v177
	v_mov_b32_e32 v3, v177
	v_mov_b32_e32 v4, v177
	v_mov_b32_e32 v5, v177
	v_mov_b32_e32 v6, v177
	v_mov_b32_e32 v7, v177
	v_mov_b32_e32 v8, v177
	v_mov_b32_e32 v9, v177
	v_mov_b32_e32 v10, v177
	v_mov_b32_e32 v11, v177
	v_mov_b32_e32 v12, v177
	v_mov_b32_e32 v13, v177
	v_mov_b32_e32 v14, v177
	v_mov_b32_e32 v15, v177
	v_mov_b32_e32 v16, v177
	v_mov_b32_e32 v17, v177
	v_mov_b32_e32 v18, v177
	v_mov_b32_e32 v19, v177
	v_mov_b32_e32 v20, v177
	v_mov_b32_e32 v21, v177
	v_mov_b32_e32 v22, v177
	v_mov_b32_e32 v23, v177
	v_mov_b32_e32 v24, v177
	v_mov_b32_e32 v25, v177
	v_mov_b32_e32 v26, v177
	v_mov_b32_e32 v27, v177
	v_mov_b32_e32 v28, v177
	v_mov_b32_e32 v29, v177
	v_mov_b32_e32 v30, v177
	v_mov_b32_e32 v31, v177
	v_mov_b32_e32 v36, v177
	v_mov_b32_e32 v37, v177
	v_mov_b32_e32 v38, v177
	v_mov_b32_e32 v39, v177
	v_mov_b32_e32 v44, v177
	v_mov_b32_e32 v45, v177
	v_mov_b32_e32 v46, v177
	v_mov_b32_e32 v47, v177
	v_mov_b32_e32 v32, v177
	v_mov_b32_e32 v33, v177
	v_mov_b32_e32 v34, v177
	v_mov_b32_e32 v35, v177
	v_mov_b32_e32 v40, v177
	v_mov_b32_e32 v41, v177
	v_mov_b32_e32 v42, v177
	v_mov_b32_e32 v43, v177
	v_mov_b32_e32 v48, v177
	v_mov_b32_e32 v49, v177
	v_mov_b32_e32 v50, v177
	v_mov_b32_e32 v51, v177
	v_mov_b32_e32 v52, v177
	v_mov_b32_e32 v53, v177
	v_mov_b32_e32 v54, v177
	v_mov_b32_e32 v55, v177
	v_mov_b32_e32 v56, v177
	v_mov_b32_e32 v57, v177
	v_mov_b32_e32 v58, v177
	v_mov_b32_e32 v59, v177
	v_mov_b32_e32 v60, v177
	v_mov_b32_e32 v61, v177
	v_mov_b32_e32 v62, v177
	v_mov_b32_e32 v63, v177
	v_mov_b32_e32 v64, v177
	v_mov_b32_e32 v65, v177
	v_mov_b32_e32 v66, v177
	v_mov_b32_e32 v67, v177
	v_mov_b32_e32 v68, v177
	v_mov_b32_e32 v69, v177
	v_mov_b32_e32 v70, v177
	v_mov_b32_e32 v71, v177
	v_mov_b32_e32 v72, v177
	v_mov_b32_e32 v73, v177
	v_mov_b32_e32 v74, v177
	v_mov_b32_e32 v75, v177
	v_mov_b32_e32 v76, v177
	v_mov_b32_e32 v77, v177
	v_mov_b32_e32 v78, v177
	v_mov_b32_e32 v79, v177
	v_mov_b32_e32 v80, v177
	v_mov_b32_e32 v81, v177
	v_mov_b32_e32 v82, v177
	v_mov_b32_e32 v83, v177
	v_mov_b32_e32 v84, v177
	v_mov_b32_e32 v85, v177
	v_mov_b32_e32 v86, v177
	v_mov_b32_e32 v87, v177
	v_mov_b32_e32 v88, v177
	v_mov_b32_e32 v89, v177
	v_mov_b32_e32 v90, v177
	v_mov_b32_e32 v91, v177
	v_mov_b32_e32 v92, v177
	v_mov_b32_e32 v93, v177
	v_mov_b32_e32 v94, v177
	v_mov_b32_e32 v95, v177
	v_mov_b32_e32 v96, v177
	v_mov_b32_e32 v97, v177
	v_mov_b32_e32 v98, v177
	v_mov_b32_e32 v99, v177
	v_mov_b32_e32 v100, v177
	v_mov_b32_e32 v101, v177
	v_mov_b32_e32 v102, v177
	v_mov_b32_e32 v103, v177
	v_mov_b32_e32 v104, v177
	v_mov_b32_e32 v105, v177
	v_mov_b32_e32 v106, v177
	v_mov_b32_e32 v107, v177
	v_mov_b32_e32 v108, v177
	v_mov_b32_e32 v109, v177
	v_mov_b32_e32 v110, v177
	v_mov_b32_e32 v111, v177
	v_mov_b32_e32 v112, v177
	v_mov_b32_e32 v113, v177
	v_mov_b32_e32 v114, v177
	v_mov_b32_e32 v115, v177
	v_mov_b32_e32 v116, v177
	v_mov_b32_e32 v117, v177
	v_mov_b32_e32 v118, v177
	v_mov_b32_e32 v119, v177
	v_mov_b32_e32 v120, v177
	v_mov_b32_e32 v121, v177
	v_mov_b32_e32 v122, v177
	v_mov_b32_e32 v123, v177
	v_mov_b32_e32 v124, v177
	v_mov_b32_e32 v125, v177
	v_mov_b32_e32 v126, v177
	v_mov_b32_e32 v127, v177
	s_barrier

.LBB0_916:
	s_add_u32 s34, s25, 0xffffff00
	s_addc_u32 s35, s27, -1
	v_readlane_b32 s42, v254, 13
	v_readlane_b32 s43, v254, 14
	v_mbcnt_lo_u32_b32 v183, -1, 0
	v_mbcnt_hi_u32_b32 v183, -1, v183
	s_bitcmp1_b32 s74, 0
	s_cselect_b32 s25, s66, 0x24c00
	s_lshl_b32 s27, s60, 2
	s_or_b32 s25, s25, s27
	v_and_b32_e32 v181, 15, v183
	v_ashrrev_i32_e32 v183, 1, v183
	v_and_b32_e32 v183, -8, v183
	v_lshl_add_u32 v179, v183, 2, s25
	ds_read_b128 v[172:175], v179
	ds_read_b128 v[160:163], v179 offset:16
	ds_read_b128 v[168:171], v179 offset:512
	ds_read_b128 v[164:167], v179 offset:528
	s_lshl_b32 s25, s48, 8
	s_add_i32 s25, s25, s59
	s_lshl_b32 s27, s4, 7
	s_or_b32 s27, s27, s60
	v_or_b32_e32 v181, s25, v181
	v_add_u32_e32 v183, s27, v183
	v_lshl_add_u32 v181, v181, 11, v183
	s_add_u32 s40, s100, s20
	s_addc_u32 s41, s101, s21
	v_mov_b32_e32 v200, 0x3b800000
	v_mov_b32_e32 v201, 0xc01d265f
	s_waitcnt lgkmcnt(0)
	v_pk_add_f32 v[168:169], v[168:169], 1.0 op_sel_hi:[1,0]
	v_pk_add_f32 v[170:171], v[170:171], 1.0 op_sel_hi:[1,0]
	v_pk_add_f32 v[164:165], v[164:165], 1.0 op_sel_hi:[1,0]
	v_pk_add_f32 v[166:167], v[166:167], 1.0 op_sel_hi:[1,0]
	v_pk_fma_f32 v[100:101], v[100:101], v[200:201], v[172:173] op_sel_hi:[1,0,1]
	v_pk_fma_f32 v[102:103], v[102:103], v[200:201], v[174:175] op_sel_hi:[1,0,1]
	v_pk_fma_f32 v[96:97], v[96:97], v[200:201], v[160:161] op_sel_hi:[1,0,1]
	v_pk_fma_f32 v[98:99], v[98:99], v[200:201], v[162:163] op_sel_hi:[1,0,1]
	v_min_f32_e32 v100, 0x40e00000, v100
	v_min_f32_e32 v101, 0x40e00000, v101
	v_min_f32_e32 v102, 0x40e00000, v102
	v_min_f32_e32 v103, 0x40e00000, v103
	v_min_f32_e32 v96, 0x40e00000, v96
	v_min_f32_e32 v97, 0x40e00000, v97
	v_min_f32_e32 v98, 0x40e00000, v98
	v_min_f32_e32 v99, 0x40e00000, v99
	v_pk_mul_f32 v[188:189], v[100:101], v[200:201] op_sel:[0,1] op_sel_hi:[1,1]
	v_pk_mul_f32 v[190:191], v[102:103], v[200:201] op_sel:[0,1] op_sel_hi:[1,1]
	v_pk_mul_f32 v[196:197], v[96:97], v[200:201] op_sel:[0,1] op_sel_hi:[1,1]
	v_pk_mul_f32 v[198:199], v[98:99], v[200:201] op_sel:[0,1] op_sel_hi:[1,1]
	v_exp_f32_e32 v188, v188
	v_exp_f32_e32 v189, v189
	v_exp_f32_e32 v190, v190
	v_exp_f32_e32 v191, v191
	v_exp_f32_e32 v196, v196
	v_exp_f32_e32 v197, v197
	v_exp_f32_e32 v198, v198
	v_exp_f32_e32 v199, v199
	v_pk_fma_f32 v[68:69], v[68:69], v[200:201], v[168:169] op_sel_hi:[1,0,1]
	v_pk_fma_f32 v[70:71], v[70:71], v[200:201], v[170:171] op_sel_hi:[1,0,1]
	v_pk_fma_f32 v[64:65], v[64:65], v[200:201], v[164:165] op_sel_hi:[1,0,1]
	v_pk_fma_f32 v[66:67], v[66:67], v[200:201], v[166:167] op_sel_hi:[1,0,1]
	v_pk_add_f32 v[188:189], v[188:189], 1.0 op_sel_hi:[1,0]
	v_pk_add_f32 v[190:191], v[190:191], 1.0 op_sel_hi:[1,0]
	v_pk_add_f32 v[196:197], v[196:197], 1.0 op_sel_hi:[1,0]
	v_pk_add_f32 v[198:199], v[198:199], 1.0 op_sel_hi:[1,0]
	v_rcp_f32_e32 v188, v188
	v_rcp_f32_e32 v189, v189
	v_rcp_f32_e32 v190, v190
	v_rcp_f32_e32 v191, v191
	v_rcp_f32_e32 v196, v196
	v_rcp_f32_e32 v197, v197
	v_rcp_f32_e32 v198, v198
	v_rcp_f32_e32 v199, v199
	v_med3_f32 v68, v68, s69, v230
	v_med3_f32 v69, v69, s69, v230
	v_med3_f32 v70, v70, s69, v230
	v_med3_f32 v71, v71, s69, v230
	v_med3_f32 v64, v64, s69, v230
	v_med3_f32 v65, v65, s69, v230
	v_med3_f32 v66, v66, s69, v230
	v_med3_f32 v67, v67, s69, v230
	v_pk_mul_f32 v[100:101], v[100:101], v[188:189]
	v_pk_mul_f32 v[102:103], v[102:103], v[190:191]
	v_pk_mul_f32 v[96:97], v[96:97], v[196:197]
	v_pk_mul_f32 v[98:99], v[98:99], v[198:199]
	v_pk_mul_f32 v[100:101], v[100:101], v[68:69]
	v_pk_mul_f32 v[102:103], v[102:103], v[70:71]
	v_pk_mul_f32 v[96:97], v[96:97], v[64:65]
	v_pk_mul_f32 v[98:99], v[98:99], v[66:67]
	v_cvt_pk_fp8_f32 v192, v100, v101
	v_cvt_pk_fp8_f32 v193, v96, v97
	v_cvt_pk_fp8_f32 v192, v102, v103 op_sel:[0,0,1]
	v_cvt_pk_fp8_f32 v193, v98, v99 op_sel:[0,0,1]
	s_nop 1
	global_store_dwordx2 v181, v[192:193], s[40:41]
	s_add_u32 s40, s40, 0x8000
	s_addc_u32 s41, s41, 0
	v_pk_fma_f32 v[92:93], v[92:93], v[200:201], v[172:173] op_sel_hi:[1,0,1]
	v_pk_fma_f32 v[94:95], v[94:95], v[200:201], v[174:175] op_sel_hi:[1,0,1]
	v_pk_fma_f32 v[88:89], v[88:89], v[200:201], v[160:161] op_sel_hi:[1,0,1]
	v_pk_fma_f32 v[90:91], v[90:91], v[200:201], v[162:163] op_sel_hi:[1,0,1]
	v_min_f32_e32 v92, 0x40e00000, v92
	v_min_f32_e32 v93, 0x40e00000, v93
	v_min_f32_e32 v94, 0x40e00000, v94
	v_min_f32_e32 v95, 0x40e00000, v95
	v_min_f32_e32 v88, 0x40e00000, v88
	v_min_f32_e32 v89, 0x40e00000, v89
	v_min_f32_e32 v90, 0x40e00000, v90
	v_min_f32_e32 v91, 0x40e00000, v91
	v_pk_mul_f32 v[188:189], v[92:93], v[200:201] op_sel:[0,1] op_sel_hi:[1,1]
	v_pk_mul_f32 v[190:191], v[94:95], v[200:201] op_sel:[0,1] op_sel_hi:[1,1]
	v_pk_mul_f32 v[196:197], v[88:89], v[200:201] op_sel:[0,1] op_sel_hi:[1,1]
	v_pk_mul_f32 v[198:199], v[90:91], v[200:201] op_sel:[0,1] op_sel_hi:[1,1]
	v_exp_f32_e32 v188, v188
	v_exp_f32_e32 v189, v189
	v_exp_f32_e32 v190, v190
	v_exp_f32_e32 v191, v191
	v_exp_f32_e32 v196, v196
	v_exp_f32_e32 v197, v197
	v_exp_f32_e32 v198, v198
	v_exp_f32_e32 v199, v199
	v_pk_fma_f32 v[60:61], v[60:61], v[200:201], v[168:169] op_sel_hi:[1,0,1]
	v_pk_fma_f32 v[62:63], v[62:63], v[200:201], v[170:171] op_sel_hi:[1,0,1]
	v_pk_fma_f32 v[56:57], v[56:57], v[200:201], v[164:165] op_sel_hi:[1,0,1]
	v_pk_fma_f32 v[58:59], v[58:59], v[200:201], v[166:167] op_sel_hi:[1,0,1]
	v_pk_add_f32 v[188:189], v[188:189], 1.0 op_sel_hi:[1,0]
	v_pk_add_f32 v[190:191], v[190:191], 1.0 op_sel_hi:[1,0]
	v_pk_add_f32 v[196:197], v[196:197], 1.0 op_sel_hi:[1,0]
	v_pk_add_f32 v[198:199], v[198:199], 1.0 op_sel_hi:[1,0]
	v_rcp_f32_e32 v188, v188
	v_rcp_f32_e32 v189, v189
	v_rcp_f32_e32 v190, v190
	v_rcp_f32_e32 v191, v191
	v_rcp_f32_e32 v196, v196
	v_rcp_f32_e32 v197, v197
	v_rcp_f32_e32 v198, v198
	v_rcp_f32_e32 v199, v199
	v_med3_f32 v60, v60, s69, v230
	v_med3_f32 v61, v61, s69, v230
	v_med3_f32 v62, v62, s69, v230
	v_med3_f32 v63, v63, s69, v230
	v_med3_f32 v56, v56, s69, v230
	v_med3_f32 v57, v57, s69, v230
	v_med3_f32 v58, v58, s69, v230
	v_med3_f32 v59, v59, s69, v230
	v_pk_mul_f32 v[92:93], v[92:93], v[188:189]
	v_pk_mul_f32 v[94:95], v[94:95], v[190:191]
	v_pk_mul_f32 v[88:89], v[88:89], v[196:197]
	v_pk_mul_f32 v[90:91], v[90:91], v[198:199]
	v_pk_mul_f32 v[92:93], v[92:93], v[60:61]
	v_pk_mul_f32 v[94:95], v[94:95], v[62:63]
	v_pk_mul_f32 v[88:89], v[88:89], v[56:57]
	v_pk_mul_f32 v[90:91], v[90:91], v[58:59]
	v_cvt_pk_fp8_f32 v192, v92, v93
	v_cvt_pk_fp8_f32 v193, v88, v89
	v_cvt_pk_fp8_f32 v192, v94, v95 op_sel:[0,0,1]
	v_cvt_pk_fp8_f32 v193, v90, v91 op_sel:[0,0,1]
	s_nop 1
	global_store_dwordx2 v181, v[192:193], s[40:41]
	s_add_u32 s40, s40, 0x8000
	s_addc_u32 s41, s41, 0
	v_pk_fma_f32 v[84:85], v[84:85], v[200:201], v[172:173] op_sel_hi:[1,0,1]
	v_pk_fma_f32 v[86:87], v[86:87], v[200:201], v[174:175] op_sel_hi:[1,0,1]
	v_pk_fma_f32 v[80:81], v[80:81], v[200:201], v[160:161] op_sel_hi:[1,0,1]
	v_pk_fma_f32 v[82:83], v[82:83], v[200:201], v[162:163] op_sel_hi:[1,0,1]
	v_min_f32_e32 v84, 0x40e00000, v84
	v_min_f32_e32 v85, 0x40e00000, v85
	v_min_f32_e32 v86, 0x40e00000, v86
	v_min_f32_e32 v87, 0x40e00000, v87
	v_min_f32_e32 v80, 0x40e00000, v80
	v_min_f32_e32 v81, 0x40e00000, v81
	v_min_f32_e32 v82, 0x40e00000, v82
	v_min_f32_e32 v83, 0x40e00000, v83
	v_pk_mul_f32 v[188:189], v[84:85], v[200:201] op_sel:[0,1] op_sel_hi:[1,1]
	v_pk_mul_f32 v[190:191], v[86:87], v[200:201] op_sel:[0,1] op_sel_hi:[1,1]
	v_pk_mul_f32 v[196:197], v[80:81], v[200:201] op_sel:[0,1] op_sel_hi:[1,1]
	v_pk_mul_f32 v[198:199], v[82:83], v[200:201] op_sel:[0,1] op_sel_hi:[1,1]
	v_exp_f32_e32 v188, v188
	v_exp_f32_e32 v189, v189
	v_exp_f32_e32 v190, v190
	v_exp_f32_e32 v191, v191
	v_exp_f32_e32 v196, v196
	v_exp_f32_e32 v197, v197
	v_exp_f32_e32 v198, v198
	v_exp_f32_e32 v199, v199
	v_pk_fma_f32 v[52:53], v[52:53], v[200:201], v[168:169] op_sel_hi:[1,0,1]
	v_pk_fma_f32 v[54:55], v[54:55], v[200:201], v[170:171] op_sel_hi:[1,0,1]
	v_pk_fma_f32 v[48:49], v[48:49], v[200:201], v[164:165] op_sel_hi:[1,0,1]
	v_pk_fma_f32 v[50:51], v[50:51], v[200:201], v[166:167] op_sel_hi:[1,0,1]
	v_pk_add_f32 v[188:189], v[188:189], 1.0 op_sel_hi:[1,0]
	v_pk_add_f32 v[190:191], v[190:191], 1.0 op_sel_hi:[1,0]
	v_pk_add_f32 v[196:197], v[196:197], 1.0 op_sel_hi:[1,0]
	v_pk_add_f32 v[198:199], v[198:199], 1.0 op_sel_hi:[1,0]
	v_rcp_f32_e32 v188, v188
	v_rcp_f32_e32 v189, v189
	v_rcp_f32_e32 v190, v190
	v_rcp_f32_e32 v191, v191
	v_rcp_f32_e32 v196, v196
	v_rcp_f32_e32 v197, v197
	v_rcp_f32_e32 v198, v198
	v_rcp_f32_e32 v199, v199
	v_med3_f32 v52, v52, s69, v230
	v_med3_f32 v53, v53, s69, v230
	v_med3_f32 v54, v54, s69, v230
	v_med3_f32 v55, v55, s69, v230
	v_med3_f32 v48, v48, s69, v230
	v_med3_f32 v49, v49, s69, v230
	v_med3_f32 v50, v50, s69, v230
	v_med3_f32 v51, v51, s69, v230
	v_pk_mul_f32 v[84:85], v[84:85], v[188:189]
	v_pk_mul_f32 v[86:87], v[86:87], v[190:191]
	v_pk_mul_f32 v[80:81], v[80:81], v[196:197]
	v_pk_mul_f32 v[82:83], v[82:83], v[198:199]
	v_pk_mul_f32 v[84:85], v[84:85], v[52:53]
	v_pk_mul_f32 v[86:87], v[86:87], v[54:55]
	v_pk_mul_f32 v[80:81], v[80:81], v[48:49]
	v_pk_mul_f32 v[82:83], v[82:83], v[50:51]
	v_cvt_pk_fp8_f32 v192, v84, v85
	v_cvt_pk_fp8_f32 v193, v80, v81
	v_cvt_pk_fp8_f32 v192, v86, v87 op_sel:[0,0,1]
	v_cvt_pk_fp8_f32 v193, v82, v83 op_sel:[0,0,1]
	s_nop 1
	global_store_dwordx2 v181, v[192:193], s[40:41]
	s_add_u32 s40, s40, 0x8000
	s_addc_u32 s41, s41, 0
	v_pk_fma_f32 v[76:77], v[76:77], v[200:201], v[172:173] op_sel_hi:[1,0,1]
	v_pk_fma_f32 v[78:79], v[78:79], v[200:201], v[174:175] op_sel_hi:[1,0,1]
	v_pk_fma_f32 v[72:73], v[72:73], v[200:201], v[160:161] op_sel_hi:[1,0,1]
	v_pk_fma_f32 v[74:75], v[74:75], v[200:201], v[162:163] op_sel_hi:[1,0,1]
	v_min_f32_e32 v76, 0x40e00000, v76
	v_min_f32_e32 v77, 0x40e00000, v77
	v_min_f32_e32 v78, 0x40e00000, v78
	v_min_f32_e32 v79, 0x40e00000, v79
	v_min_f32_e32 v72, 0x40e00000, v72
	v_min_f32_e32 v73, 0x40e00000, v73
	v_min_f32_e32 v74, 0x40e00000, v74
	v_min_f32_e32 v75, 0x40e00000, v75
	v_pk_mul_f32 v[188:189], v[76:77], v[200:201] op_sel:[0,1] op_sel_hi:[1,1]
	v_pk_mul_f32 v[190:191], v[78:79], v[200:201] op_sel:[0,1] op_sel_hi:[1,1]
	v_pk_mul_f32 v[196:197], v[72:73], v[200:201] op_sel:[0,1] op_sel_hi:[1,1]
	v_pk_mul_f32 v[198:199], v[74:75], v[200:201] op_sel:[0,1] op_sel_hi:[1,1]
	v_exp_f32_e32 v188, v188
	v_exp_f32_e32 v189, v189
	v_exp_f32_e32 v190, v190
	v_exp_f32_e32 v191, v191
	v_exp_f32_e32 v196, v196
	v_exp_f32_e32 v197, v197
	v_exp_f32_e32 v198, v198
	v_exp_f32_e32 v199, v199
	v_pk_fma_f32 v[40:41], v[40:41], v[200:201], v[168:169] op_sel_hi:[1,0,1]
	v_pk_fma_f32 v[42:43], v[42:43], v[200:201], v[170:171] op_sel_hi:[1,0,1]
	v_pk_fma_f32 v[32:33], v[32:33], v[200:201], v[164:165] op_sel_hi:[1,0,1]
	v_pk_fma_f32 v[34:35], v[34:35], v[200:201], v[166:167] op_sel_hi:[1,0,1]
	v_pk_add_f32 v[188:189], v[188:189], 1.0 op_sel_hi:[1,0]
	v_pk_add_f32 v[190:191], v[190:191], 1.0 op_sel_hi:[1,0]
	v_pk_add_f32 v[196:197], v[196:197], 1.0 op_sel_hi:[1,0]
	v_pk_add_f32 v[198:199], v[198:199], 1.0 op_sel_hi:[1,0]
	v_rcp_f32_e32 v188, v188
	v_rcp_f32_e32 v189, v189
	v_rcp_f32_e32 v190, v190
	v_rcp_f32_e32 v191, v191
	v_rcp_f32_e32 v196, v196
	v_rcp_f32_e32 v197, v197
	v_rcp_f32_e32 v198, v198
	v_rcp_f32_e32 v199, v199
	v_med3_f32 v40, v40, s69, v230
	v_med3_f32 v41, v41, s69, v230
	v_med3_f32 v42, v42, s69, v230
	v_med3_f32 v43, v43, s69, v230
	v_med3_f32 v32, v32, s69, v230
	v_med3_f32 v33, v33, s69, v230
	v_med3_f32 v34, v34, s69, v230
	v_med3_f32 v35, v35, s69, v230
	v_pk_mul_f32 v[76:77], v[76:77], v[188:189]
	v_pk_mul_f32 v[78:79], v[78:79], v[190:191]
	v_pk_mul_f32 v[72:73], v[72:73], v[196:197]
	v_pk_mul_f32 v[74:75], v[74:75], v[198:199]
	v_pk_mul_f32 v[76:77], v[76:77], v[40:41]
	v_pk_mul_f32 v[78:79], v[78:79], v[42:43]
	v_pk_mul_f32 v[72:73], v[72:73], v[32:33]
	v_pk_mul_f32 v[74:75], v[74:75], v[34:35]
	v_cvt_pk_fp8_f32 v192, v76, v77
	v_cvt_pk_fp8_f32 v193, v72, v73
	v_cvt_pk_fp8_f32 v192, v78, v79 op_sel:[0,0,1]
	v_cvt_pk_fp8_f32 v193, v74, v75 op_sel:[0,0,1]
	s_nop 1
	global_store_dwordx2 v181, v[192:193], s[40:41]
	s_add_u32 s40, s40, 0x28000
	s_addc_u32 s41, s41, 0
	v_pk_fma_f32 v[44:45], v[44:45], v[200:201], v[172:173] op_sel_hi:[1,0,1]
	v_pk_fma_f32 v[46:47], v[46:47], v[200:201], v[174:175] op_sel_hi:[1,0,1]
	v_pk_fma_f32 v[36:37], v[36:37], v[200:201], v[160:161] op_sel_hi:[1,0,1]
	v_pk_fma_f32 v[38:39], v[38:39], v[200:201], v[162:163] op_sel_hi:[1,0,1]
	v_min_f32_e32 v44, 0x40e00000, v44
	v_min_f32_e32 v45, 0x40e00000, v45
	v_min_f32_e32 v46, 0x40e00000, v46
	v_min_f32_e32 v47, 0x40e00000, v47
	v_min_f32_e32 v36, 0x40e00000, v36
	v_min_f32_e32 v37, 0x40e00000, v37
	v_min_f32_e32 v38, 0x40e00000, v38
	v_min_f32_e32 v39, 0x40e00000, v39
	v_pk_mul_f32 v[188:189], v[44:45], v[200:201] op_sel:[0,1] op_sel_hi:[1,1]
	v_pk_mul_f32 v[190:191], v[46:47], v[200:201] op_sel:[0,1] op_sel_hi:[1,1]
	v_pk_mul_f32 v[196:197], v[36:37], v[200:201] op_sel:[0,1] op_sel_hi:[1,1]
	v_pk_mul_f32 v[198:199], v[38:39], v[200:201] op_sel:[0,1] op_sel_hi:[1,1]
	v_exp_f32_e32 v188, v188
	v_exp_f32_e32 v189, v189
	v_exp_f32_e32 v190, v190
	v_exp_f32_e32 v191, v191
	v_exp_f32_e32 v196, v196
	v_exp_f32_e32 v197, v197
	v_exp_f32_e32 v198, v198
	v_exp_f32_e32 v199, v199
	v_pk_fma_f32 v[4:5], v[4:5], v[200:201], v[168:169] op_sel_hi:[1,0,1]
	v_pk_fma_f32 v[6:7], v[6:7], v[200:201], v[170:171] op_sel_hi:[1,0,1]
	v_pk_fma_f32 v[0:1], v[0:1], v[200:201], v[164:165] op_sel_hi:[1,0,1]
	v_pk_fma_f32 v[2:3], v[2:3], v[200:201], v[166:167] op_sel_hi:[1,0,1]
	v_pk_add_f32 v[188:189], v[188:189], 1.0 op_sel_hi:[1,0]
	v_pk_add_f32 v[190:191], v[190:191], 1.0 op_sel_hi:[1,0]
	v_pk_add_f32 v[196:197], v[196:197], 1.0 op_sel_hi:[1,0]
	v_pk_add_f32 v[198:199], v[198:199], 1.0 op_sel_hi:[1,0]
	v_rcp_f32_e32 v188, v188
	v_rcp_f32_e32 v189, v189
	v_rcp_f32_e32 v190, v190
	v_rcp_f32_e32 v191, v191
	v_rcp_f32_e32 v196, v196
	v_rcp_f32_e32 v197, v197
	v_rcp_f32_e32 v198, v198
	v_rcp_f32_e32 v199, v199
	v_med3_f32 v4, v4, s69, v230
	v_med3_f32 v5, v5, s69, v230
	v_med3_f32 v6, v6, s69, v230
	v_med3_f32 v7, v7, s69, v230
	v_med3_f32 v0, v0, s69, v230
	v_med3_f32 v1, v1, s69, v230
	v_med3_f32 v2, v2, s69, v230
	v_med3_f32 v3, v3, s69, v230
	v_pk_mul_f32 v[44:45], v[44:45], v[188:189]
	v_pk_mul_f32 v[46:47], v[46:47], v[190:191]
	v_pk_mul_f32 v[36:37], v[36:37], v[196:197]
	v_pk_mul_f32 v[38:39], v[38:39], v[198:199]
	v_pk_mul_f32 v[44:45], v[44:45], v[4:5]
	v_pk_mul_f32 v[46:47], v[46:47], v[6:7]
	v_pk_mul_f32 v[36:37], v[36:37], v[0:1]
	v_pk_mul_f32 v[38:39], v[38:39], v[2:3]
	v_cvt_pk_fp8_f32 v192, v44, v45
	v_cvt_pk_fp8_f32 v193, v36, v37
	v_cvt_pk_fp8_f32 v192, v46, v47 op_sel:[0,0,1]
	v_cvt_pk_fp8_f32 v193, v38, v39 op_sel:[0,0,1]
	s_nop 1
	global_store_dwordx2 v181, v[192:193], s[40:41]
	s_add_u32 s40, s40, 0x8000
	s_addc_u32 s41, s41, 0
	v_pk_fma_f32 v[28:29], v[28:29], v[200:201], v[172:173] op_sel_hi:[1,0,1]
	v_pk_fma_f32 v[30:31], v[30:31], v[200:201], v[174:175] op_sel_hi:[1,0,1]
	v_pk_fma_f32 v[24:25], v[24:25], v[200:201], v[160:161] op_sel_hi:[1,0,1]
	v_pk_fma_f32 v[26:27], v[26:27], v[200:201], v[162:163] op_sel_hi:[1,0,1]
	v_min_f32_e32 v28, 0x40e00000, v28
	v_min_f32_e32 v29, 0x40e00000, v29
	v_min_f32_e32 v30, 0x40e00000, v30
	v_min_f32_e32 v31, 0x40e00000, v31
	v_min_f32_e32 v24, 0x40e00000, v24
	v_min_f32_e32 v25, 0x40e00000, v25
	v_min_f32_e32 v26, 0x40e00000, v26
	v_min_f32_e32 v27, 0x40e00000, v27
	v_pk_mul_f32 v[188:189], v[28:29], v[200:201] op_sel:[0,1] op_sel_hi:[1,1]
	v_pk_mul_f32 v[190:191], v[30:31], v[200:201] op_sel:[0,1] op_sel_hi:[1,1]
	v_pk_mul_f32 v[196:197], v[24:25], v[200:201] op_sel:[0,1] op_sel_hi:[1,1]
	v_pk_mul_f32 v[198:199], v[26:27], v[200:201] op_sel:[0,1] op_sel_hi:[1,1]
	v_exp_f32_e32 v188, v188
	v_exp_f32_e32 v189, v189
	v_exp_f32_e32 v190, v190
	v_exp_f32_e32 v191, v191
	v_exp_f32_e32 v196, v196
	v_exp_f32_e32 v197, v197
	v_exp_f32_e32 v198, v198
	v_exp_f32_e32 v199, v199
	v_pk_fma_f32 v[104:105], v[104:105], v[200:201], v[168:169] op_sel_hi:[1,0,1]
	v_pk_fma_f32 v[106:107], v[106:107], v[200:201], v[170:171] op_sel_hi:[1,0,1]
	v_pk_fma_f32 v[108:109], v[108:109], v[200:201], v[164:165] op_sel_hi:[1,0,1]
	v_pk_fma_f32 v[110:111], v[110:111], v[200:201], v[166:167] op_sel_hi:[1,0,1]
	v_pk_add_f32 v[188:189], v[188:189], 1.0 op_sel_hi:[1,0]
	v_pk_add_f32 v[190:191], v[190:191], 1.0 op_sel_hi:[1,0]
	v_pk_add_f32 v[196:197], v[196:197], 1.0 op_sel_hi:[1,0]
	v_pk_add_f32 v[198:199], v[198:199], 1.0 op_sel_hi:[1,0]
	v_rcp_f32_e32 v188, v188
	v_rcp_f32_e32 v189, v189
	v_rcp_f32_e32 v190, v190
	v_rcp_f32_e32 v191, v191
	v_rcp_f32_e32 v196, v196
	v_rcp_f32_e32 v197, v197
	v_rcp_f32_e32 v198, v198
	v_rcp_f32_e32 v199, v199
	v_med3_f32 v104, v104, s69, v230
	v_med3_f32 v105, v105, s69, v230
	v_med3_f32 v106, v106, s69, v230
	v_med3_f32 v107, v107, s69, v230
	v_med3_f32 v108, v108, s69, v230
	v_med3_f32 v109, v109, s69, v230
	v_med3_f32 v110, v110, s69, v230
	v_med3_f32 v111, v111, s69, v230
	v_pk_mul_f32 v[28:29], v[28:29], v[188:189]
	v_pk_mul_f32 v[30:31], v[30:31], v[190:191]
	v_pk_mul_f32 v[24:25], v[24:25], v[196:197]
	v_pk_mul_f32 v[26:27], v[26:27], v[198:199]
	v_pk_mul_f32 v[28:29], v[28:29], v[104:105]
	v_pk_mul_f32 v[30:31], v[30:31], v[106:107]
	v_pk_mul_f32 v[24:25], v[24:25], v[108:109]
	v_pk_mul_f32 v[26:27], v[26:27], v[110:111]
	v_cvt_pk_fp8_f32 v192, v28, v29
	v_cvt_pk_fp8_f32 v193, v24, v25
	v_cvt_pk_fp8_f32 v192, v30, v31 op_sel:[0,0,1]
	v_cvt_pk_fp8_f32 v193, v26, v27 op_sel:[0,0,1]
	s_nop 1
	global_store_dwordx2 v181, v[192:193], s[40:41]
	s_add_u32 s40, s40, 0x8000
	s_addc_u32 s41, s41, 0
	v_pk_fma_f32 v[20:21], v[20:21], v[200:201], v[172:173] op_sel_hi:[1,0,1]
	v_pk_fma_f32 v[22:23], v[22:23], v[200:201], v[174:175] op_sel_hi:[1,0,1]
	v_pk_fma_f32 v[16:17], v[16:17], v[200:201], v[160:161] op_sel_hi:[1,0,1]
	v_pk_fma_f32 v[18:19], v[18:19], v[200:201], v[162:163] op_sel_hi:[1,0,1]
	v_min_f32_e32 v20, 0x40e00000, v20
	v_min_f32_e32 v21, 0x40e00000, v21
	v_min_f32_e32 v22, 0x40e00000, v22
	v_min_f32_e32 v23, 0x40e00000, v23
	v_min_f32_e32 v16, 0x40e00000, v16
	v_min_f32_e32 v17, 0x40e00000, v17
	v_min_f32_e32 v18, 0x40e00000, v18
	v_min_f32_e32 v19, 0x40e00000, v19
	v_pk_mul_f32 v[188:189], v[20:21], v[200:201] op_sel:[0,1] op_sel_hi:[1,1]
	v_pk_mul_f32 v[190:191], v[22:23], v[200:201] op_sel:[0,1] op_sel_hi:[1,1]
	v_pk_mul_f32 v[196:197], v[16:17], v[200:201] op_sel:[0,1] op_sel_hi:[1,1]
	v_pk_mul_f32 v[198:199], v[18:19], v[200:201] op_sel:[0,1] op_sel_hi:[1,1]
	v_exp_f32_e32 v188, v188
	v_exp_f32_e32 v189, v189
	v_exp_f32_e32 v190, v190
	v_exp_f32_e32 v191, v191
	v_exp_f32_e32 v196, v196
	v_exp_f32_e32 v197, v197
	v_exp_f32_e32 v198, v198
	v_exp_f32_e32 v199, v199
	v_pk_fma_f32 v[112:113], v[112:113], v[200:201], v[168:169] op_sel_hi:[1,0,1]
	v_pk_fma_f32 v[114:115], v[114:115], v[200:201], v[170:171] op_sel_hi:[1,0,1]
	v_pk_fma_f32 v[116:117], v[116:117], v[200:201], v[164:165] op_sel_hi:[1,0,1]
	v_pk_fma_f32 v[118:119], v[118:119], v[200:201], v[166:167] op_sel_hi:[1,0,1]
	v_pk_add_f32 v[188:189], v[188:189], 1.0 op_sel_hi:[1,0]
	v_pk_add_f32 v[190:191], v[190:191], 1.0 op_sel_hi:[1,0]
	v_pk_add_f32 v[196:197], v[196:197], 1.0 op_sel_hi:[1,0]
	v_pk_add_f32 v[198:199], v[198:199], 1.0 op_sel_hi:[1,0]
	v_rcp_f32_e32 v188, v188
	v_rcp_f32_e32 v189, v189
	v_rcp_f32_e32 v190, v190
	v_rcp_f32_e32 v191, v191
	v_rcp_f32_e32 v196, v196
	v_rcp_f32_e32 v197, v197
	v_rcp_f32_e32 v198, v198
	v_rcp_f32_e32 v199, v199
	v_med3_f32 v112, v112, s69, v230
	v_med3_f32 v113, v113, s69, v230
	v_med3_f32 v114, v114, s69, v230
	v_med3_f32 v115, v115, s69, v230
	v_med3_f32 v116, v116, s69, v230
	v_med3_f32 v117, v117, s69, v230
	v_med3_f32 v118, v118, s69, v230
	v_med3_f32 v119, v119, s69, v230
	v_pk_mul_f32 v[20:21], v[20:21], v[188:189]
	v_pk_mul_f32 v[22:23], v[22:23], v[190:191]
	v_pk_mul_f32 v[16:17], v[16:17], v[196:197]
	v_pk_mul_f32 v[18:19], v[18:19], v[198:199]
	v_pk_mul_f32 v[20:21], v[20:21], v[112:113]
	v_pk_mul_f32 v[22:23], v[22:23], v[114:115]
	v_pk_mul_f32 v[16:17], v[16:17], v[116:117]
	v_pk_mul_f32 v[18:19], v[18:19], v[118:119]
	v_cvt_pk_fp8_f32 v192, v20, v21
	v_cvt_pk_fp8_f32 v193, v16, v17
	v_cvt_pk_fp8_f32 v192, v22, v23 op_sel:[0,0,1]
	v_cvt_pk_fp8_f32 v193, v18, v19 op_sel:[0,0,1]
	s_nop 1
	global_store_dwordx2 v181, v[192:193], s[40:41]
	s_add_u32 s40, s40, 0x8000
	s_addc_u32 s41, s41, 0
	v_pk_fma_f32 v[12:13], v[12:13], v[200:201], v[172:173] op_sel_hi:[1,0,1]
	v_pk_fma_f32 v[14:15], v[14:15], v[200:201], v[174:175] op_sel_hi:[1,0,1]
	v_pk_fma_f32 v[8:9], v[8:9], v[200:201], v[160:161] op_sel_hi:[1,0,1]
	v_pk_fma_f32 v[10:11], v[10:11], v[200:201], v[162:163] op_sel_hi:[1,0,1]
	v_min_f32_e32 v12, 0x40e00000, v12
	v_min_f32_e32 v13, 0x40e00000, v13
	v_min_f32_e32 v14, 0x40e00000, v14
	v_min_f32_e32 v15, 0x40e00000, v15
	v_min_f32_e32 v8, 0x40e00000, v8
	v_min_f32_e32 v9, 0x40e00000, v9
	v_min_f32_e32 v10, 0x40e00000, v10
	v_min_f32_e32 v11, 0x40e00000, v11
	v_pk_mul_f32 v[188:189], v[12:13], v[200:201] op_sel:[0,1] op_sel_hi:[1,1]
	v_pk_mul_f32 v[190:191], v[14:15], v[200:201] op_sel:[0,1] op_sel_hi:[1,1]
	v_pk_mul_f32 v[196:197], v[8:9], v[200:201] op_sel:[0,1] op_sel_hi:[1,1]
	v_pk_mul_f32 v[198:199], v[10:11], v[200:201] op_sel:[0,1] op_sel_hi:[1,1]
	v_exp_f32_e32 v188, v188
	v_exp_f32_e32 v189, v189
	v_exp_f32_e32 v190, v190
	v_exp_f32_e32 v191, v191
	v_exp_f32_e32 v196, v196
	v_exp_f32_e32 v197, v197
	v_exp_f32_e32 v198, v198
	v_exp_f32_e32 v199, v199
	v_pk_fma_f32 v[120:121], v[120:121], v[200:201], v[168:169] op_sel_hi:[1,0,1]
	v_pk_fma_f32 v[122:123], v[122:123], v[200:201], v[170:171] op_sel_hi:[1,0,1]
	v_pk_fma_f32 v[124:125], v[124:125], v[200:201], v[164:165] op_sel_hi:[1,0,1]
	v_pk_fma_f32 v[126:127], v[126:127], v[200:201], v[166:167] op_sel_hi:[1,0,1]
	v_pk_add_f32 v[188:189], v[188:189], 1.0 op_sel_hi:[1,0]
	v_pk_add_f32 v[190:191], v[190:191], 1.0 op_sel_hi:[1,0]
	v_pk_add_f32 v[196:197], v[196:197], 1.0 op_sel_hi:[1,0]
	v_pk_add_f32 v[198:199], v[198:199], 1.0 op_sel_hi:[1,0]
	v_rcp_f32_e32 v188, v188
	v_rcp_f32_e32 v189, v189
	v_rcp_f32_e32 v190, v190
	v_rcp_f32_e32 v191, v191
	v_rcp_f32_e32 v196, v196
	v_rcp_f32_e32 v197, v197
	v_rcp_f32_e32 v198, v198
	v_rcp_f32_e32 v199, v199
	v_med3_f32 v120, v120, s69, v230
	v_med3_f32 v121, v121, s69, v230
	v_med3_f32 v122, v122, s69, v230
	v_med3_f32 v123, v123, s69, v230
	v_med3_f32 v124, v124, s69, v230
	v_med3_f32 v125, v125, s69, v230
	v_med3_f32 v126, v126, s69, v230
	v_med3_f32 v127, v127, s69, v230
	v_pk_mul_f32 v[12:13], v[12:13], v[188:189]
	v_pk_mul_f32 v[14:15], v[14:15], v[190:191]
	v_pk_mul_f32 v[8:9], v[8:9], v[196:197]
	v_pk_mul_f32 v[10:11], v[10:11], v[198:199]
	v_pk_mul_f32 v[12:13], v[12:13], v[120:121]
	v_pk_mul_f32 v[14:15], v[14:15], v[122:123]
	v_pk_mul_f32 v[8:9], v[8:9], v[124:125]
	v_pk_mul_f32 v[10:11], v[10:11], v[126:127]
	v_cvt_pk_fp8_f32 v192, v12, v13
	v_cvt_pk_fp8_f32 v193, v8, v9
	v_cvt_pk_fp8_f32 v192, v14, v15 op_sel:[0,0,1]
	v_cvt_pk_fp8_f32 v193, v10, v11 op_sel:[0,0,1]
	s_nop 1
	global_store_dwordx2 v181, v[192:193], s[40:41]
	s_nop 0
	s_mov_b64 s[40:41], s[100:101]
	s_waitcnt vmcnt(8)
	v_pk_mul_f32 v[128:129], v[128:129], v[252:253]
	v_pk_mul_f32 v[130:131], v[130:131], v[252:253]
	v_pk_mul_f32 v[132:133], v[132:133], v[252:253]
	v_pk_mul_f32 v[134:135], v[134:135], v[252:253]
	v_pk_mul_f32 v[136:137], v[136:137], v[252:253]
	v_pk_mul_f32 v[138:139], v[138:139], v[252:253]
	v_pk_mul_f32 v[140:141], v[140:141], v[252:253]
	v_pk_mul_f32 v[142:143], v[142:143], v[252:253]
	v_pk_mul_f32 v[144:145], v[144:145], v[252:253]
	v_pk_mul_f32 v[146:147], v[146:147], v[252:253]
	v_pk_mul_f32 v[148:149], v[148:149], v[252:253]
	v_pk_mul_f32 v[150:151], v[150:151], v[252:253]
	v_pk_mul_f32 v[152:153], v[152:153], v[252:253]
	v_pk_mul_f32 v[154:155], v[154:155], v[252:253]
	v_pk_mul_f32 v[156:157], v[156:157], v[252:253]
	v_pk_mul_f32 v[158:159], v[158:159], v[252:253]
	v_cvt_pk_fp8_f32 v166, v128, v132
	v_cvt_pk_fp8_f32 v167, v144, v148
	v_cvt_pk_fp8_f32 v168, v129, v133
	v_cvt_pk_fp8_f32 v169, v145, v149
	v_cvt_pk_fp8_f32 v170, v130, v134
	v_cvt_pk_fp8_f32 v171, v146, v150
	v_cvt_pk_fp8_f32 v172, v131, v135
	v_cvt_pk_fp8_f32 v173, v147, v151
	v_cvt_pk_fp8_f32 v166, v136, v140 op_sel:[0,0,1]
	v_cvt_pk_fp8_f32 v167, v152, v156 op_sel:[0,0,1]
	v_cvt_pk_fp8_f32 v168, v137, v141 op_sel:[0,0,1]
	v_cvt_pk_fp8_f32 v169, v153, v157 op_sel:[0,0,1]
	v_cvt_pk_fp8_f32 v170, v138, v142 op_sel:[0,0,1]
	v_cvt_pk_fp8_f32 v171, v154, v158 op_sel:[0,0,1]
	v_cvt_pk_fp8_f32 v172, v139, v143 op_sel:[0,0,1]
	v_cvt_pk_fp8_f32 v173, v155, v159 op_sel:[0,0,1]
	s_lshl_b32 s25, s38, 16
	s_mov_b64 s[38:39], s[42:43]
	v_mbcnt_lo_u32_b32 v160, -1, 0
	v_mbcnt_hi_u32_b32 v160, -1, v160
	s_mov_b64 s[38:39], s[100:101]
	s_and_b32 s25, s25, 0x3f0000
	s_lshl_b64 s[36:37], s[36:37], 22
	v_and_b32_e32 v161, -8, v160
	v_lshlrev_b32_e32 v160, 13, v160
	s_waitcnt lgkmcnt(0)
	s_add_u32 s36, s38, s36
	v_and_b32_e32 v160, 0xe000, v160
	s_addc_u32 s37, s39, s37
	s_or_b32 s7, s25, s7
	v_add3_u32 v160, s7, v161, v160
	v_mov_b32_e32 v161, v177
	v_lshl_add_u64 v[160:161], s[36:37], 0, v[160:161]
	v_lshl_add_u64 v[162:163], v[160:161], 0, s[22:23]
	v_add_co_u32_e32 v160, vcc, s70, v160
	s_nop 1
	v_addc_co_u32_e32 v161, vcc, 0, v161, vcc
	s_and_b64 vcc, exec, s[2:3]
	global_store_dwordx2 v[160:161], v[166:167], off offset:-4096
	global_store_dwordx2 v[162:163], v[168:169], off offset:2048
	global_store_dwordx2 v[160:161], v[170:171], off
	global_store_dwordx2 v[160:161], v[172:173], off offset:2048
	s_cbranch_vccnz .LBB0_920
	s_andn2_b64 vcc, exec, s[0:1]
	s_cbranch_vccnz .LBB0_919
	s_barrier
